# v39_ldmove
# baseline (speedup 1.0000x reference)
.LBB3_12:
	s_or_b64 exec, exec, s[20:21]
	v_mov_b32_e32 v107, v67
	ds_write_b128 v123, v[22:25] offset:35776
	ds_write_b128 v124, v[26:29] offset:40896
	ds_write_b128 v125, v[30:33] offset:46016
	ds_write_b128 v126, v[34:37] offset:51136
	ds_write_b128 v127, v[38:41] offset:56256
	v_lshl_add_u64 v[22:23], s[56:57], 0, v[106:107]
	v_add_co_u32_e32 v24, vcc, 0xc000, v22
	s_waitcnt lgkmcnt(0)
	s_nop 0
	v_addc_co_u32_e32 v25, vcc, 0, v23, vcc
	v_add_co_u32_e32 v28, vcc, 0xd000, v22
	s_barrier
	v_add_u32_e32 v196, 0x6f80, v129
	v_add_u32_e32 v197, 0x6f80, v123
	v_add_u32_e32 v198, 0x6f80, v124
	v_add_u32_e32 v199, 0x6f80, v125
	v_add_u32_e32 v200, 0x6f80, v126
	v_add_u32_e32 v201, 0x6f80, v127
	s_nop 0
	v_addc_co_u32_e32 v29, vcc, 0, v23, vcc
	v_add_co_u32_e32 v32, vcc, 0xf000, v22
	s_nop 1
	v_addc_co_u32_e32 v33, vcc, 0, v23, vcc
	v_add_co_u32_e32 v36, vcc, 0x10000, v22
	global_load_dwordx4 v[24:27], v[24:25], off offset:2048
	s_nop 0
	global_load_dwordx4 v[28:31], v[28:29], off offset:3072
	v_addc_co_u32_e32 v37, vcc, 0, v23, vcc
	v_add_co_u32_e32 v40, vcc, 0x11000, v22
	global_load_dwordx4 v[32:35], v[32:33], off
	s_nop 0
	global_load_dwordx4 v[36:39], v[36:37], off offset:1024
	v_addc_co_u32_e32 v41, vcc, 0, v23, vcc
	global_load_dwordx4 v[40:43], v[40:41], off offset:2048
	ds_write_b128 v197, v[2:5] offset:35776
	ds_write_b128 v198, v[6:9] offset:40896
	ds_write_b128 v199, v[10:13] offset:46016
	ds_write_b128 v200, v[14:17] offset:51136
	ds_write_b128 v201, v[18:21] offset:56256
	s_waitcnt vmcnt(5)
	ds_read_b128 v[44:47], v129 offset:35776
	ds_read_b128 v[48:51], v144
	ds_read_b128 v[52:55], v144 offset:64
	ds_read_b128 v[56:59], v129 offset:35840
	ds_read_b128 v[60:63], v129 offset:42432
	ds_read_b128 v[152:155], v129 offset:42496
	ds_read_b128 v[156:159], v129 offset:49088
	ds_read_b128 v[160:163], v129 offset:49152
	s_waitcnt lgkmcnt(6)
	v_mfma_f32_16x16x32_f16 v[44:47], v[44:47], v[48:51], 0
	ds_read_b128 v[164:167], v129 offset:55744
	ds_read_b128 v[168:171], v129 offset:55808
	s_waitcnt lgkmcnt(5)
	v_mfma_f32_16x16x32_f16 v[60:63], v[60:63], v[48:51], 0
	v_mfma_f32_16x16x32_f16 v[44:47], v[56:59], v[52:55], v[44:47]
	s_waitcnt lgkmcnt(4)
	v_mfma_f32_16x16x32_f16 v[56:59], v[152:155], v[52:55], v[60:63]
	ds_read_b128 v[152:155], v129 offset:35904
	s_waitcnt lgkmcnt(4)
	v_mfma_f32_16x16x32_f16 v[156:159], v[156:159], v[48:51], 0
	s_waitcnt lgkmcnt(2)
	v_mfma_f32_16x16x32_f16 v[48:51], v[164:167], v[48:51], 0
	v_mfma_f32_16x16x32_f16 v[60:63], v[160:163], v[52:55], v[156:159]
	s_waitcnt lgkmcnt(1)
	v_mfma_f32_16x16x32_f16 v[48:51], v[168:171], v[52:55], v[48:51]
	ds_read_b128 v[52:55], v144 offset:128
	s_nop 1
	ds_read_b128 v[156:159], v144 offset:192
	ds_read_b128 v[160:163], v129 offset:35968
	s_waitcnt lgkmcnt(2)
	v_mfma_f32_16x16x32_f16 v[44:47], v[152:155], v[52:55], v[44:47]
	ds_read_b128 v[152:155], v129 offset:42560
	ds_read_b128 v[164:167], v129 offset:42624
	s_waitcnt lgkmcnt(1)
	v_mfma_f32_16x16x32_f16 v[56:59], v[152:155], v[52:55], v[56:59]
	ds_read_b128 v[152:155], v129 offset:49216
	ds_read_b128 v[168:171], v129 offset:49280
	s_waitcnt lgkmcnt(1)
	v_mfma_f32_16x16x32_f16 v[60:63], v[152:155], v[52:55], v[60:63]
	ds_read_b128 v[152:155], v129 offset:55872
	ds_read_b128 v[172:175], v129 offset:55936
	s_waitcnt lgkmcnt(1)
	v_mfma_f32_16x16x32_f16 v[48:51], v[152:155], v[52:55], v[48:51]
	v_mfma_f32_16x16x32_f16 v[44:47], v[160:163], v[156:159], v[44:47]
	ds_read_b128 v[52:55], v144 offset:256
	ds_read_b128 v[152:155], v144 offset:320
	ds_read_b128 v[160:163], v129 offset:36032
	ds_read_b128 v[176:179], v129 offset:36096
	v_mfma_f32_16x16x32_f16 v[56:59], v[164:167], v[156:159], v[56:59]
	ds_read_b128 v[164:167], v129 offset:42688
	ds_read_b128 v[180:183], v129 offset:42752
	ds_read_b128 v[184:187], v129 offset:49344
	ds_read_b128 v[188:191], v129 offset:49408
	v_mfma_f32_16x16x32_f16 v[60:63], v[168:171], v[156:159], v[60:63]
	ds_read_b128 v[168:171], v129 offset:56000
	ds_read_b128 v[192:195], v129 offset:56064
	s_waitcnt lgkmcnt(0)
	v_mfma_f32_16x16x32_f16 v[48:51], v[172:175], v[156:159], v[48:51]
	v_add_co_u32_e32 v18, vcc, s75, v22
	v_mfma_f32_16x16x32_f16 v[2:5], v[160:163], v[52:55], v[44:47]
	s_nop 0
	v_addc_co_u32_e32 v19, vcc, 0, v23, vcc
	s_waitcnt lgkmcnt(0)
	v_add_co_u32_e32 v44, vcc, s76, v22
	v_mfma_f32_16x16x32_f16 v[14:17], v[168:171], v[52:55], v[48:51]
	s_nop 0
	v_addc_co_u32_e32 v45, vcc, 0, v23, vcc
	s_barrier
	v_add_co_u32_e32 v48, vcc, s77, v22
	v_mfma_f32_16x16x32_f16 v[6:9], v[164:167], v[52:55], v[56:59]
	s_nop 0
	v_addc_co_u32_e32 v49, vcc, 0, v23, vcc
	v_mfma_f32_16x16x32_f16 v[10:13], v[184:187], v[52:55], v[60:63]
	v_add_co_u32_e32 v52, vcc, s78, v22
	global_load_dwordx4 v[18:21], v[18:19], off offset:3072
	s_nop 0
	global_load_dwordx4 v[44:47], v[44:45], off
	v_addc_co_u32_e32 v53, vcc, 0, v23, vcc
	v_add_co_u32_e32 v56, vcc, s79, v22
	global_load_dwordx4 v[48:51], v[48:49], off offset:1024
	s_nop 0
	global_load_dwordx4 v[52:55], v[52:53], off offset:2048
	v_addc_co_u32_e32 v57, vcc, 0, v23, vcc
	global_load_dwordx4 v[56:59], v[56:57], off offset:3072
	s_waitcnt vmcnt(9)
	ds_write_b128 v123, v[24:27] offset:35776
	s_waitcnt vmcnt(8)
	ds_write_b128 v124, v[28:31] offset:40896
	s_waitcnt vmcnt(7)
	ds_write_b128 v125, v[32:35] offset:46016
	s_waitcnt vmcnt(6)
	ds_write_b128 v126, v[36:39] offset:51136
	s_waitcnt vmcnt(5)
	ds_write_b128 v127, v[40:43] offset:56256
	v_mfma_f32_16x16x32_f16 v[2:5], v[176:179], v[152:155], v[2:5]
	v_mfma_f32_16x16x32_f16 v[6:9], v[180:183], v[152:155], v[6:9]
	v_mfma_f32_16x16x32_f16 v[10:13], v[188:191], v[152:155], v[10:13]
	v_mfma_f32_16x16x32_f16 v[14:17], v[192:195], v[152:155], v[14:17]
	ds_read_b128 v[60:63], v196 offset:35776
	ds_read_b128 v[152:155], v144 offset:416
	ds_read_b128 v[208:211], v196 offset:42432
	ds_read_b128 v[212:215], v196 offset:49088
	ds_read_b128 v[216:219], v196 offset:55744
	ds_read_b128 v[156:159], v144 offset:480
	ds_read_b128 v[160:163], v196 offset:35840
	ds_read_b128 v[164:167], v196 offset:42496
	ds_read_b128 v[168:171], v196 offset:49152
	ds_read_b128 v[172:175], v196 offset:55808
	s_waitcnt lgkmcnt(8)
	v_mfma_f32_16x16x32_f16 v[2:5], v[60:63], v[152:155], v[2:5]
	s_waitcnt lgkmcnt(7)
	v_mfma_f32_16x16x32_f16 v[6:9], v[208:211], v[152:155], v[6:9]
	s_waitcnt lgkmcnt(6)
	v_mfma_f32_16x16x32_f16 v[10:13], v[212:215], v[152:155], v[10:13]
	s_waitcnt lgkmcnt(5)
	v_mfma_f32_16x16x32_f16 v[14:17], v[216:219], v[152:155], v[14:17]
	s_waitcnt lgkmcnt(0)
	ds_read_b128 v[60:63], v196 offset:35904
	v_mfma_f32_16x16x32_f16 v[2:5], v[160:163], v[156:159], v[2:5]
	v_mfma_f32_16x16x32_f16 v[6:9], v[164:167], v[156:159], v[6:9]
	v_mfma_f32_16x16x32_f16 v[10:13], v[168:171], v[156:159], v[10:13]
	s_waitcnt lgkmcnt(1)
	v_mfma_f32_16x16x32_f16 v[14:17], v[172:175], v[156:159], v[14:17]
	ds_read_b128 v[152:155], v144 offset:544
	ds_read_b128 v[208:211], v196 offset:42560
	ds_read_b128 v[212:215], v196 offset:49216
	ds_read_b128 v[216:219], v196 offset:55872
	ds_read_b128 v[156:159], v144 offset:608
	ds_read_b128 v[160:163], v196 offset:35968
	ds_read_b128 v[164:167], v196 offset:42624
	ds_read_b128 v[168:171], v196 offset:49280
	ds_read_b128 v[172:175], v196 offset:55936
	s_waitcnt lgkmcnt(8)
	v_mfma_f32_16x16x32_f16 v[2:5], v[60:63], v[152:155], v[2:5]
	s_waitcnt lgkmcnt(7)
	v_mfma_f32_16x16x32_f16 v[6:9], v[208:211], v[152:155], v[6:9]
	s_waitcnt lgkmcnt(6)
	v_mfma_f32_16x16x32_f16 v[10:13], v[212:215], v[152:155], v[10:13]
	s_waitcnt lgkmcnt(5)
	v_mfma_f32_16x16x32_f16 v[14:17], v[216:219], v[152:155], v[14:17]
	s_waitcnt lgkmcnt(0)
	v_mfma_f32_16x16x32_f16 v[2:5], v[160:163], v[156:159], v[2:5]
	ds_read_b128 v[60:63], v144 offset:672
	ds_read_b128 v[152:155], v144 offset:736
	ds_read_b128 v[160:163], v196 offset:36032
	ds_read_b128 v[176:179], v196 offset:36096
	v_mfma_f32_16x16x32_f16 v[6:9], v[164:167], v[156:159], v[6:9]
	ds_read_b128 v[164:167], v196 offset:42688
	ds_read_b128 v[180:183], v196 offset:42752
	ds_read_b128 v[184:187], v196 offset:49344
	ds_read_b128 v[188:191], v196 offset:49408
	v_mfma_f32_16x16x32_f16 v[10:13], v[168:171], v[156:159], v[10:13]
	ds_read_b128 v[168:171], v196 offset:56000
	ds_read_b128 v[192:195], v196 offset:56064
	s_waitcnt lgkmcnt(0)
	s_waitcnt lgkmcnt(0)
	s_barrier
	s_waitcnt vmcnt(4)
	ds_write_b128 v197, v[18:21] offset:35776
	s_waitcnt vmcnt(3)
	ds_write_b128 v198, v[44:47] offset:40896
	s_waitcnt vmcnt(2)
	ds_write_b128 v199, v[48:51] offset:46016
	s_waitcnt vmcnt(1)
	ds_write_b128 v200, v[52:55] offset:51136
	s_waitcnt vmcnt(0)
	ds_write_b128 v201, v[56:59] offset:56256
	v_mfma_f32_16x16x32_f16 v[14:17], v[172:175], v[156:159], v[14:17]
	v_mfma_f32_16x16x32_f16 v[2:5], v[160:163], v[60:63], v[2:5]
	v_mfma_f32_16x16x32_f16 v[6:9], v[164:167], v[60:63], v[6:9]
	v_mfma_f32_16x16x32_f16 v[10:13], v[184:187], v[60:63], v[10:13]
	v_mfma_f32_16x16x32_f16 v[14:17], v[168:171], v[60:63], v[14:17]
	v_mfma_f32_16x16x32_f16 v[2:5], v[176:179], v[152:155], v[2:5]
	v_mfma_f32_16x16x32_f16 v[6:9], v[180:183], v[152:155], v[6:9]
	v_mfma_f32_16x16x32_f16 v[10:13], v[188:191], v[152:155], v[10:13]
	v_mfma_f32_16x16x32_f16 v[14:17], v[192:195], v[152:155], v[14:17]
	ds_read_b128 v[60:63], v129 offset:35776
	ds_read_b128 v[152:155], v144 offset:832
	ds_read_b128 v[208:211], v129 offset:42432
	ds_read_b128 v[212:215], v129 offset:49088
	ds_read_b128 v[216:219], v129 offset:55744
	ds_read_b128 v[156:159], v144 offset:896
	ds_read_b128 v[160:163], v129 offset:35840
	ds_read_b128 v[164:167], v129 offset:42496
	ds_read_b128 v[168:171], v129 offset:49152
	ds_read_b128 v[172:175], v129 offset:55808
	s_waitcnt lgkmcnt(8)
	v_mfma_f32_16x16x32_f16 v[2:5], v[60:63], v[152:155], v[2:5]
	s_waitcnt lgkmcnt(7)
	v_mfma_f32_16x16x32_f16 v[6:9], v[208:211], v[152:155], v[6:9]
	s_waitcnt lgkmcnt(6)
	v_mfma_f32_16x16x32_f16 v[10:13], v[212:215], v[152:155], v[10:13]
	s_waitcnt lgkmcnt(5)
	v_mfma_f32_16x16x32_f16 v[14:17], v[216:219], v[152:155], v[14:17]
	s_waitcnt lgkmcnt(0)
	v_add_co_u32_e32 v24, vcc, s80, v22
	v_addc_co_u32_e32 v25, vcc, 0, v23, vcc
	v_add_co_u32_e32 v28, vcc, s81, v22
	s_nop 0
	v_addc_co_u32_e32 v29, vcc, 0, v23, vcc
	v_add_co_u32_e32 v32, vcc, s82, v22
	s_nop 0
	v_addc_co_u32_e32 v33, vcc, 0, v23, vcc
	v_add_co_u32_e32 v36, vcc, s83, v22
	s_nop 1
	v_addc_co_u32_e32 v37, vcc, 0, v23, vcc
	v_add_co_u32_e32 v40, vcc, s84, v22
	global_load_dwordx4 v[24:27], v[24:25], off
	s_nop 0
	global_load_dwordx4 v[28:31], v[28:29], off offset:1024
	s_nop 0
	global_load_dwordx4 v[32:35], v[32:33], off offset:2048
	s_nop 0
	global_load_dwordx4 v[36:39], v[36:37], off offset:3072
	v_addc_co_u32_e32 v41, vcc, 0, v23, vcc
	global_load_dwordx4 v[40:43], v[40:41], off
	ds_read_b128 v[60:63], v129 offset:35904
	v_mfma_f32_16x16x32_f16 v[2:5], v[160:163], v[156:159], v[2:5]
	v_mfma_f32_16x16x32_f16 v[6:9], v[164:167], v[156:159], v[6:9]
	v_mfma_f32_16x16x32_f16 v[10:13], v[168:171], v[156:159], v[10:13]
	s_waitcnt lgkmcnt(1)
	v_mfma_f32_16x16x32_f16 v[14:17], v[172:175], v[156:159], v[14:17]
	ds_read_b128 v[152:155], v144 offset:960
	ds_read_b128 v[208:211], v129 offset:42560
	ds_read_b128 v[212:215], v129 offset:49216
	ds_read_b128 v[216:219], v129 offset:55872
	ds_read_b128 v[156:159], v144 offset:1024
	ds_read_b128 v[160:163], v129 offset:35968
	ds_read_b128 v[164:167], v129 offset:42624
	ds_read_b128 v[168:171], v129 offset:49280
	ds_read_b128 v[172:175], v129 offset:55936
	s_waitcnt lgkmcnt(8)
	v_mfma_f32_16x16x32_f16 v[2:5], v[60:63], v[152:155], v[2:5]
	s_waitcnt lgkmcnt(7)
	v_mfma_f32_16x16x32_f16 v[6:9], v[208:211], v[152:155], v[6:9]
	s_waitcnt lgkmcnt(6)
	v_mfma_f32_16x16x32_f16 v[10:13], v[212:215], v[152:155], v[10:13]
	s_waitcnt lgkmcnt(5)
	v_mfma_f32_16x16x32_f16 v[14:17], v[216:219], v[152:155], v[14:17]
	s_waitcnt lgkmcnt(0)
	v_mfma_f32_16x16x32_f16 v[2:5], v[160:163], v[156:159], v[2:5]
	ds_read_b128 v[60:63], v144 offset:1088
	ds_read_b128 v[152:155], v144 offset:1152
	ds_read_b128 v[160:163], v129 offset:36032
	ds_read_b128 v[176:179], v129 offset:36096
	v_mfma_f32_16x16x32_f16 v[6:9], v[164:167], v[156:159], v[6:9]
	ds_read_b128 v[164:167], v129 offset:42688
	ds_read_b128 v[180:183], v129 offset:42752
	ds_read_b128 v[184:187], v129 offset:49344
	ds_read_b128 v[188:191], v129 offset:49408
	v_mfma_f32_16x16x32_f16 v[10:13], v[168:171], v[156:159], v[10:13]
	ds_read_b128 v[168:171], v129 offset:56000
	ds_read_b128 v[192:195], v129 offset:56064
	s_waitcnt lgkmcnt(0)
	s_waitcnt lgkmcnt(0)
	s_barrier
	s_waitcnt vmcnt(4)
	ds_write_b128 v123, v[24:27] offset:35776
	s_waitcnt vmcnt(3)
	ds_write_b128 v124, v[28:31] offset:40896
	s_waitcnt vmcnt(2)
	ds_write_b128 v125, v[32:35] offset:46016
	s_waitcnt vmcnt(1)
	ds_write_b128 v126, v[36:39] offset:51136
	s_waitcnt vmcnt(0)
	ds_write_b128 v127, v[40:43] offset:56256
	v_mfma_f32_16x16x32_f16 v[14:17], v[172:175], v[156:159], v[14:17]
	v_mfma_f32_16x16x32_f16 v[2:5], v[160:163], v[60:63], v[2:5]
	v_mfma_f32_16x16x32_f16 v[6:9], v[164:167], v[60:63], v[6:9]
	v_mfma_f32_16x16x32_f16 v[10:13], v[184:187], v[60:63], v[10:13]
	v_mfma_f32_16x16x32_f16 v[14:17], v[168:171], v[60:63], v[14:17]
	v_mfma_f32_16x16x32_f16 v[2:5], v[176:179], v[152:155], v[2:5]
	v_mfma_f32_16x16x32_f16 v[6:9], v[180:183], v[152:155], v[6:9]
	v_mfma_f32_16x16x32_f16 v[10:13], v[188:191], v[152:155], v[10:13]
	v_mfma_f32_16x16x32_f16 v[14:17], v[192:195], v[152:155], v[14:17]
	ds_read_b128 v[60:63], v196 offset:35776
	ds_read_b128 v[152:155], v144 offset:1248
	ds_read_b128 v[208:211], v196 offset:42432
	ds_read_b128 v[212:215], v196 offset:49088
	ds_read_b128 v[216:219], v196 offset:55744
	ds_read_b128 v[156:159], v144 offset:1312
	ds_read_b128 v[160:163], v196 offset:35840
	ds_read_b128 v[164:167], v196 offset:42496
	ds_read_b128 v[168:171], v196 offset:49152
	ds_read_b128 v[172:175], v196 offset:55808
	s_waitcnt lgkmcnt(8)
	v_mfma_f32_16x16x32_f16 v[2:5], v[60:63], v[152:155], v[2:5]
	s_waitcnt lgkmcnt(7)
	v_mfma_f32_16x16x32_f16 v[6:9], v[208:211], v[152:155], v[6:9]
	s_waitcnt lgkmcnt(6)
	v_mfma_f32_16x16x32_f16 v[10:13], v[212:215], v[152:155], v[10:13]
	s_waitcnt lgkmcnt(5)
	v_mfma_f32_16x16x32_f16 v[14:17], v[216:219], v[152:155], v[14:17]
	s_waitcnt lgkmcnt(0)
	v_add_co_u32_e32 v18, vcc, s85, v22
	v_addc_co_u32_e32 v19, vcc, 0, v23, vcc
	v_add_co_u32_e32 v44, vcc, s27, v22
	s_nop 0
	v_addc_co_u32_e32 v45, vcc, 0, v23, vcc
	v_add_co_u32_e32 v48, vcc, s86, v22
	s_nop 0
	v_addc_co_u32_e32 v49, vcc, 0, v23, vcc
	v_add_co_u32_e32 v52, vcc, s87, v22
	s_nop 1
	v_addc_co_u32_e32 v53, vcc, 0, v23, vcc
	v_add_co_u32_e32 v56, vcc, s88, v22
	global_load_dwordx4 v[18:21], v[18:19], off offset:1024
	s_nop 0
	global_load_dwordx4 v[44:47], v[44:45], off offset:2048
	s_nop 0
	global_load_dwordx4 v[48:51], v[48:49], off offset:3072
	s_nop 0
	global_load_dwordx4 v[52:55], v[52:53], off
	v_addc_co_u32_e32 v57, vcc, 0, v23, vcc
	global_load_dwordx4 v[56:59], v[56:57], off offset:1024
	ds_read_b128 v[60:63], v196 offset:35904
	v_mfma_f32_16x16x32_f16 v[2:5], v[160:163], v[156:159], v[2:5]
	v_mfma_f32_16x16x32_f16 v[6:9], v[164:167], v[156:159], v[6:9]
	v_mfma_f32_16x16x32_f16 v[10:13], v[168:171], v[156:159], v[10:13]
	s_waitcnt lgkmcnt(1)
	v_mfma_f32_16x16x32_f16 v[14:17], v[172:175], v[156:159], v[14:17]
	ds_read_b128 v[152:155], v144 offset:1376
	ds_read_b128 v[208:211], v196 offset:42560
	ds_read_b128 v[212:215], v196 offset:49216
	ds_read_b128 v[216:219], v196 offset:55872
	ds_read_b128 v[156:159], v144 offset:1440
	ds_read_b128 v[160:163], v196 offset:35968
	ds_read_b128 v[164:167], v196 offset:42624
	ds_read_b128 v[168:171], v196 offset:49280
	ds_read_b128 v[172:175], v196 offset:55936
	s_waitcnt lgkmcnt(8)
	v_mfma_f32_16x16x32_f16 v[2:5], v[60:63], v[152:155], v[2:5]
	s_waitcnt lgkmcnt(7)
	v_mfma_f32_16x16x32_f16 v[6:9], v[208:211], v[152:155], v[6:9]
	s_waitcnt lgkmcnt(6)
	v_mfma_f32_16x16x32_f16 v[10:13], v[212:215], v[152:155], v[10:13]
	s_waitcnt lgkmcnt(5)
	v_mfma_f32_16x16x32_f16 v[14:17], v[216:219], v[152:155], v[14:17]
	s_waitcnt lgkmcnt(0)
	v_mfma_f32_16x16x32_f16 v[2:5], v[160:163], v[156:159], v[2:5]
	ds_read_b128 v[60:63], v144 offset:1504
	ds_read_b128 v[152:155], v144 offset:1568
	ds_read_b128 v[160:163], v196 offset:36032
	ds_read_b128 v[176:179], v196 offset:36096
	v_mfma_f32_16x16x32_f16 v[6:9], v[164:167], v[156:159], v[6:9]
	ds_read_b128 v[164:167], v196 offset:42688
	ds_read_b128 v[180:183], v196 offset:42752
	ds_read_b128 v[184:187], v196 offset:49344
	ds_read_b128 v[188:191], v196 offset:49408
	v_mfma_f32_16x16x32_f16 v[10:13], v[168:171], v[156:159], v[10:13]
	ds_read_b128 v[168:171], v196 offset:56000
	ds_read_b128 v[192:195], v196 offset:56064
	s_waitcnt lgkmcnt(0)
	s_waitcnt lgkmcnt(0)
	s_barrier
	s_waitcnt vmcnt(4)
	ds_write_b128 v197, v[18:21] offset:35776
	s_waitcnt vmcnt(3)
	ds_write_b128 v198, v[44:47] offset:40896
	s_waitcnt vmcnt(2)
	ds_write_b128 v199, v[48:51] offset:46016
	s_waitcnt vmcnt(1)
	ds_write_b128 v200, v[52:55] offset:51136
	s_waitcnt vmcnt(0)
	ds_write_b128 v201, v[56:59] offset:56256
	v_mfma_f32_16x16x32_f16 v[14:17], v[172:175], v[156:159], v[14:17]
	v_mfma_f32_16x16x32_f16 v[2:5], v[160:163], v[60:63], v[2:5]
	v_mfma_f32_16x16x32_f16 v[6:9], v[164:167], v[60:63], v[6:9]
	v_mfma_f32_16x16x32_f16 v[10:13], v[184:187], v[60:63], v[10:13]
	v_mfma_f32_16x16x32_f16 v[14:17], v[168:171], v[60:63], v[14:17]
	v_mfma_f32_16x16x32_f16 v[2:5], v[176:179], v[152:155], v[2:5]
	v_mfma_f32_16x16x32_f16 v[6:9], v[180:183], v[152:155], v[6:9]
	v_mfma_f32_16x16x32_f16 v[10:13], v[188:191], v[152:155], v[10:13]
	v_mfma_f32_16x16x32_f16 v[14:17], v[192:195], v[152:155], v[14:17]
	ds_read_b128 v[60:63], v129 offset:35776
	ds_read_b128 v[152:155], v144 offset:1664
	ds_read_b128 v[208:211], v129 offset:42432
	ds_read_b128 v[212:215], v129 offset:49088
	ds_read_b128 v[216:219], v129 offset:55744
	ds_read_b128 v[156:159], v144 offset:1728
	ds_read_b128 v[160:163], v129 offset:35840
	ds_read_b128 v[164:167], v129 offset:42496
	ds_read_b128 v[168:171], v129 offset:49152
	ds_read_b128 v[172:175], v129 offset:55808
	s_waitcnt lgkmcnt(8)
	v_mfma_f32_16x16x32_f16 v[2:5], v[60:63], v[152:155], v[2:5]
	s_waitcnt lgkmcnt(7)
	v_mfma_f32_16x16x32_f16 v[6:9], v[208:211], v[152:155], v[6:9]
	s_waitcnt lgkmcnt(6)
	v_mfma_f32_16x16x32_f16 v[10:13], v[212:215], v[152:155], v[10:13]
	s_waitcnt lgkmcnt(5)
	v_mfma_f32_16x16x32_f16 v[14:17], v[216:219], v[152:155], v[14:17]
	s_waitcnt lgkmcnt(0)
	v_add_co_u32_e32 v24, vcc, s89, v22
	v_addc_co_u32_e32 v25, vcc, 0, v23, vcc
	v_add_co_u32_e32 v28, vcc, s90, v22
	s_nop 0
	v_addc_co_u32_e32 v29, vcc, 0, v23, vcc
	v_add_co_u32_e32 v32, vcc, s91, v22
	s_nop 0
	v_addc_co_u32_e32 v33, vcc, 0, v23, vcc
	v_add_co_u32_e32 v36, vcc, s92, v22
	s_nop 1
	v_addc_co_u32_e32 v37, vcc, 0, v23, vcc
	v_add_co_u32_e32 v22, vcc, s93, v22
	global_load_dwordx4 v[24:27], v[24:25], off offset:2048
	s_nop 0
	global_load_dwordx4 v[28:31], v[28:29], off offset:3072
	s_nop 0
	global_load_dwordx4 v[32:35], v[32:33], off
	s_nop 0
	global_load_dwordx4 v[36:39], v[36:37], off offset:1024
	v_addc_co_u32_e32 v23, vcc, 0, v23, vcc
	global_load_dwordx4 v[40:43], v[22:23], off offset:2048
	ds_read_b128 v[60:63], v129 offset:35904
	v_mfma_f32_16x16x32_f16 v[2:5], v[160:163], v[156:159], v[2:5]
	v_mfma_f32_16x16x32_f16 v[6:9], v[164:167], v[156:159], v[6:9]
	v_mfma_f32_16x16x32_f16 v[10:13], v[168:171], v[156:159], v[10:13]
	s_waitcnt lgkmcnt(1)
	v_mfma_f32_16x16x32_f16 v[14:17], v[172:175], v[156:159], v[14:17]
	ds_read_b128 v[152:155], v144 offset:1792
	ds_read_b128 v[208:211], v129 offset:42560
	ds_read_b128 v[212:215], v129 offset:49216
	ds_read_b128 v[216:219], v129 offset:55872
	ds_read_b128 v[156:159], v144 offset:1856
	ds_read_b128 v[160:163], v129 offset:35968
	ds_read_b128 v[164:167], v129 offset:42624
	ds_read_b128 v[168:171], v129 offset:49280
	ds_read_b128 v[172:175], v129 offset:55936
	s_waitcnt lgkmcnt(8)
	v_mfma_f32_16x16x32_f16 v[2:5], v[60:63], v[152:155], v[2:5]
	s_waitcnt lgkmcnt(7)
	v_mfma_f32_16x16x32_f16 v[6:9], v[208:211], v[152:155], v[6:9]
	s_waitcnt lgkmcnt(6)
	v_mfma_f32_16x16x32_f16 v[10:13], v[212:215], v[152:155], v[10:13]
	s_waitcnt lgkmcnt(5)
	v_mfma_f32_16x16x32_f16 v[14:17], v[216:219], v[152:155], v[14:17]
	s_waitcnt lgkmcnt(0)
	ds_read_b128 v[60:63], v129 offset:36032
	v_mfma_f32_16x16x32_f16 v[2:5], v[160:163], v[156:159], v[2:5]
	v_mfma_f32_16x16x32_f16 v[6:9], v[164:167], v[156:159], v[6:9]
	v_mfma_f32_16x16x32_f16 v[10:13], v[168:171], v[156:159], v[10:13]
	s_waitcnt lgkmcnt(1)
	v_mfma_f32_16x16x32_f16 v[14:17], v[172:175], v[156:159], v[14:17]
	ds_read_b128 v[152:155], v144 offset:1920
	ds_read_b128 v[156:159], v144 offset:1984
	ds_read_b128 v[160:163], v129 offset:36096
	s_waitcnt lgkmcnt(2)
	v_mfma_f32_16x16x32_f16 v[2:5], v[60:63], v[152:155], v[2:5]
	ds_read_b128 v[60:63], v129 offset:42688
	ds_read_b128 v[164:167], v129 offset:42752
	s_waitcnt lgkmcnt(1)
	v_mfma_f32_16x16x32_f16 v[6:9], v[60:63], v[152:155], v[6:9]
	ds_read_b128 v[60:63], v129 offset:49344
	ds_read_b128 v[168:171], v129 offset:49408
	s_waitcnt lgkmcnt(1)
	v_mfma_f32_16x16x32_f16 v[10:13], v[60:63], v[152:155], v[10:13]
	ds_read_b128 v[60:63], v129 offset:56000
	ds_read_b128 v[172:175], v129 offset:56064
	s_waitcnt lgkmcnt(0)
	v_mfma_f32_16x16x32_f16 v[14:17], v[60:63], v[152:155], v[14:17]
	v_mfma_f32_16x16x32_f16 v[2:5], v[160:163], v[156:159], v[2:5]
	s_waitcnt lgkmcnt(0)
	s_barrier
	s_waitcnt vmcnt(4)
	ds_write_b128 v123, v[24:27] offset:35776
	s_waitcnt vmcnt(3)
	ds_write_b128 v124, v[28:31] offset:40896
	s_waitcnt vmcnt(2)
	ds_write_b128 v125, v[32:35] offset:46016
	s_waitcnt vmcnt(1)
	ds_write_b128 v126, v[36:39] offset:51136
	s_waitcnt vmcnt(0)
	ds_write_b128 v127, v[40:43] offset:56256
	v_mfma_f32_16x16x32_f16 v[6:9], v[164:167], v[156:159], v[6:9]
	v_mfma_f32_16x16x32_f16 v[10:13], v[168:171], v[156:159], v[10:13]
	v_mfma_f32_16x16x32_f16 v[14:17], v[172:175], v[156:159], v[14:17]
	ds_read_b128 v[18:21], v196 offset:35776
	ds_read_b128 v[44:47], v144 offset:2080
	ds_read_b128 v[48:51], v144 offset:2144
	ds_read_b128 v[52:55], v196 offset:35840
	s_waitcnt lgkmcnt(2)
	v_mfma_f32_16x16x32_f16 v[2:5], v[18:21], v[44:47], v[2:5]
	ds_read_b128 v[18:21], v196 offset:42432
	ds_read_b128 v[56:59], v196 offset:42496
	s_waitcnt lgkmcnt(1)
	v_mfma_f32_16x16x32_f16 v[6:9], v[18:21], v[44:47], v[6:9]
	ds_read_b128 v[18:21], v196 offset:49088
	ds_read_b128 v[60:63], v196 offset:49152
	s_waitcnt lgkmcnt(1)
	v_mfma_f32_16x16x32_f16 v[10:13], v[18:21], v[44:47], v[10:13]
	ds_read_b128 v[18:21], v196 offset:55744
	ds_read_b128 v[152:155], v196 offset:55808
	s_waitcnt lgkmcnt(1)
	v_mfma_f32_16x16x32_f16 v[14:17], v[18:21], v[44:47], v[14:17]
	ds_read_b128 v[18:21], v196 offset:35904
	v_mfma_f32_16x16x32_f16 v[2:5], v[52:55], v[48:51], v[2:5]
	v_mfma_f32_16x16x32_f16 v[6:9], v[56:59], v[48:51], v[6:9]
	v_mfma_f32_16x16x32_f16 v[10:13], v[60:63], v[48:51], v[10:13]
	s_waitcnt lgkmcnt(1)
	v_mfma_f32_16x16x32_f16 v[14:17], v[152:155], v[48:51], v[14:17]
	ds_read_b128 v[44:47], v144 offset:2208
	ds_read_b128 v[48:51], v144 offset:2272
	ds_read_b128 v[52:55], v196 offset:35968
	s_waitcnt lgkmcnt(2)
	v_mfma_f32_16x16x32_f16 v[2:5], v[18:21], v[44:47], v[2:5]
	ds_read_b128 v[18:21], v196 offset:42560
	ds_read_b128 v[56:59], v196 offset:42624
	s_waitcnt lgkmcnt(1)
	v_mfma_f32_16x16x32_f16 v[6:9], v[18:21], v[44:47], v[6:9]
	ds_read_b128 v[18:21], v196 offset:49216
	ds_read_b128 v[60:63], v196 offset:49280
	s_waitcnt lgkmcnt(1)
	v_mfma_f32_16x16x32_f16 v[10:13], v[18:21], v[44:47], v[10:13]
	ds_read_b128 v[18:21], v196 offset:55872
	ds_read_b128 v[152:155], v196 offset:55936
	s_waitcnt lgkmcnt(1)
	v_mfma_f32_16x16x32_f16 v[14:17], v[18:21], v[44:47], v[14:17]
	ds_read_b128 v[18:21], v196 offset:36032
	v_mfma_f32_16x16x32_f16 v[2:5], v[52:55], v[48:51], v[2:5]
	v_mfma_f32_16x16x32_f16 v[6:9], v[56:59], v[48:51], v[6:9]
	v_mfma_f32_16x16x32_f16 v[10:13], v[60:63], v[48:51], v[10:13]
	s_waitcnt lgkmcnt(1)
	v_mfma_f32_16x16x32_f16 v[14:17], v[152:155], v[48:51], v[14:17]
	ds_read_b128 v[44:47], v144 offset:2336
	ds_read_b128 v[48:51], v144 offset:2400
	ds_read_b128 v[52:55], v196 offset:36096
	s_waitcnt lgkmcnt(2)
	v_mfma_f32_16x16x32_f16 v[2:5], v[18:21], v[44:47], v[2:5]
	ds_read_b128 v[18:21], v196 offset:42688
	ds_read_b128 v[56:59], v196 offset:42752
	s_waitcnt lgkmcnt(1)
	v_mfma_f32_16x16x32_f16 v[6:9], v[18:21], v[44:47], v[6:9]
	ds_read_b128 v[18:21], v196 offset:49344
	ds_read_b128 v[60:63], v196 offset:49408
	s_waitcnt lgkmcnt(1)
	v_mfma_f32_16x16x32_f16 v[10:13], v[18:21], v[44:47], v[10:13]
	ds_read_b128 v[18:21], v196 offset:56000
	ds_read_b128 v[152:155], v196 offset:56064
	s_waitcnt lgkmcnt(0)
	v_mfma_f32_16x16x32_f16 v[14:17], v[18:21], v[44:47], v[14:17]
	v_mfma_f32_16x16x32_f16 v[2:5], v[52:55], v[48:51], v[2:5]
	s_waitcnt lgkmcnt(0)
	s_barrier
	v_mfma_f32_16x16x32_f16 v[6:9], v[56:59], v[48:51], v[6:9]
	v_mfma_f32_16x16x32_f16 v[10:13], v[60:63], v[48:51], v[10:13]
	v_mfma_f32_16x16x32_f16 v[14:17], v[152:155], v[48:51], v[14:17]
	ds_read_b128 v[18:21], v129 offset:35776
	ds_read_b128 v[22:25], v144 offset:2496
	ds_read_b128 v[26:29], v144 offset:2560
	ds_read_b128 v[30:33], v129 offset:35840
	s_waitcnt lgkmcnt(2)
	v_mfma_f32_16x16x32_f16 v[2:5], v[18:21], v[22:25], v[2:5]
	ds_read_b128 v[18:21], v129 offset:42432
	ds_read_b128 v[34:37], v129 offset:42496
	s_waitcnt lgkmcnt(1)
	v_mfma_f32_16x16x32_f16 v[6:9], v[18:21], v[22:25], v[6:9]
	ds_read_b128 v[18:21], v129 offset:49088
	ds_read_b128 v[38:41], v129 offset:49152
	s_waitcnt lgkmcnt(1)
	v_mfma_f32_16x16x32_f16 v[10:13], v[18:21], v[22:25], v[10:13]
	ds_read_b128 v[18:21], v129 offset:55744
	ds_read_b128 v[42:45], v129 offset:55808
	s_waitcnt lgkmcnt(1)
	v_mfma_f32_16x16x32_f16 v[14:17], v[18:21], v[22:25], v[14:17]
	v_mfma_f32_16x16x32_f16 v[2:5], v[30:33], v[26:29], v[2:5]
	ds_read_b128 v[18:21], v144 offset:2624
	ds_read_b128 v[22:25], v144 offset:2688
	ds_read_b128 v[30:33], v129 offset:35904
	ds_read_b128 v[46:49], v129 offset:35968
	s_waitcnt lgkmcnt(1)
	v_mfma_f32_16x16x32_f16 v[2:5], v[30:33], v[18:21], v[2:5]
	v_mfma_f32_16x16x32_f16 v[6:9], v[34:37], v[26:29], v[6:9]
	ds_read_b128 v[34:37], v129 offset:42560
	ds_read_b128 v[50:53], v129 offset:42624
	ds_read_b128 v[54:57], v129 offset:49216
	ds_read_b128 v[58:61], v129 offset:49280
	v_mfma_f32_16x16x32_f16 v[10:13], v[38:41], v[26:29], v[10:13]
	ds_read_b128 v[38:41], v129 offset:55872
	ds_read_b128 v[62:65], v129 offset:55936
	ds_read_b128 v[152:155], v129 offset:36032
	ds_read_b128 v[30:33], v144 offset:2752
	ds_read_b128 v[156:159], v144 offset:2816
	ds_read_b128 v[160:163], v129 offset:36096
	s_waitcnt lgkmcnt(10)
	v_mfma_f32_16x16x32_f16 v[2:5], v[46:49], v[22:25], v[2:5]
	ds_read_b128 v[46:49], v129 offset:42688
	ds_read_b128 v[164:167], v129 offset:42752
	ds_read_b128 v[168:171], v129 offset:49344
	ds_read_b128 v[172:175], v129 offset:49408
	s_waitcnt lgkmcnt(6)
	v_mfma_f32_16x16x32_f16 v[2:5], v[152:155], v[30:33], v[2:5]
	ds_read_b128 v[152:155], v129 offset:56000
	ds_read_b128 v[176:179], v129 offset:56064
	ds_read_b128 v[180:183], v98 offset:63808
	ds_read_b128 v[184:187], v98 offset:64064
	s_waitcnt lgkmcnt(8)
	v_mfma_f32_16x16x32_f16 v[2:5], v[160:163], v[156:159], v[2:5]
	ds_read_b128 v[160:163], v98 offset:63872
	ds_read_b128 v[188:191], v98 offset:64128
	v_mfma_f32_16x16x32_f16 v[14:17], v[42:45], v[26:29], v[14:17]
	s_waitcnt lgkmcnt(2)
	s_nop 3
	v_pk_fma_f32 v[2:3], v[2:3], v[180:181], v[184:185]
	s_nop 0
	v_pk_mul_f32 v[26:27], v[2:3], s[28:29] op_sel_hi:[1,0]
	v_mfma_f32_16x16x32_f16 v[6:9], v[34:37], v[18:21], v[6:9]
	v_mul_f32_e64 v29, |v26|, -|v26|
	v_mul_f32_e32 v29, 0x3fb8aa3b, v29
	v_fma_f32 v28, |v26|, s74, 1.0
	v_exp_f32_e32 v34, v29
	v_fma_f32 v29, |v27|, s74, 1.0
	v_rcp_f32_e32 v28, v28
	v_rcp_f32_e32 v29, v29
	v_mfma_f32_16x16x32_f16 v[10:13], v[54:57], v[18:21], v[10:13]
	v_mul_f32_e64 v35, |v27|, -|v27|
	v_mul_f32_e32 v35, 0x3fb8aa3b, v35
	v_exp_f32_e32 v35, v35
	v_mfma_f32_16x16x32_f16 v[16:19], v[38:41], v[18:21], v[14:17]
	v_mul_f32_e64 v2, v2, 0.5
	v_mul_f32_e64 v3, v3, 0.5
	s_nop 0
	v_mov_b64_e32 v[14:15], s[34:35]
	v_pk_fma_f32 v[20:21], v[28:29], s[40:41], v[14:15] op_sel_hi:[1,0,0]
	v_mfma_f32_16x16x32_f16 v[10:13], v[58:61], v[22:25], v[10:13]
	v_fma_f32 v20, v28, v20, s42
	v_fma_f32 v21, v29, v21, s42
	v_pk_fma_f32 v[20:21], v[28:29], v[20:21], s[44:45] op_sel_hi:[1,1,0]
	v_mfma_f32_16x16x32_f16 v[6:9], v[50:53], v[22:25], v[6:9]
	v_fma_f32 v20, v28, v20, s46
	v_fma_f32 v21, v29, v21, s46
	v_pk_mul_f32 v[20:21], v[20:21], v[28:29] neg_lo:[0,1] neg_hi:[0,1]
	v_mfma_f32_16x16x32_f16 v[16:19], v[62:65], v[22:25], v[16:19]
	v_fma_f32 v20, v20, v34, 1.0
	v_fma_f32 v21, v21, v35, 1.0
	v_bfi_b32 v21, s71, v21, v27
	v_bfi_b32 v20, s71, v20, v26
	v_pk_fma_f32 v[26:27], v[4:5], v[182:183], v[186:187]
	v_pk_add_f32 v[20:21], v[20:21], 1.0 op_sel_hi:[1,0]
	v_pk_mul_f32 v[28:29], v[26:27], s[28:29] op_sel_hi:[1,0]
	v_pk_mul_f32 v[24:25], v[2:3], v[20:21]
	v_mfma_f32_16x16x32_f16 v[2:5], v[168:171], v[30:33], v[10:13]
	v_mul_f32_e64 v26, v26, 0.5
	v_mul_f32_e64 v27, v27, 0.5
	s_nop 0
	v_fma_f32 v10, |v28|, s74, 1.0
	v_fma_f32 v11, |v29|, s74, 1.0
	v_rcp_f32_e32 v34, v10
	v_rcp_f32_e32 v35, v11
	v_mul_f32_e64 v10, |v28|, -|v28|
	v_mul_f32_e32 v10, 0x3fb8aa3b, v10
	v_mfma_f32_16x16x32_f16 v[6:9], v[46:49], v[30:33], v[6:9]
	v_mfma_f32_16x16x32_f16 v[16:19], v[152:155], v[30:33], v[16:19]
	v_exp_f32_e32 v30, v10
	v_mfma_f32_16x16x32_f16 v[10:13], v[172:175], v[156:159], v[2:5]
	s_nop 2
	v_mul_f32_e64 v4, |v29|, -|v29|
	v_pk_fma_f32 v[2:3], v[34:35], s[40:41], v[14:15] op_sel_hi:[1,0,0]
	v_mul_f32_e32 v4, 0x3fb8aa3b, v4
	v_pk_fma_f32 v[2:3], v[34:35], v[2:3], s[42:43] op_sel_hi:[1,1,0]
	v_exp_f32_e32 v31, v4
	v_pk_fma_f32 v[2:3], v[34:35], v[2:3], s[44:45] op_sel_hi:[1,1,0]
	v_mfma_f32_16x16x32_f16 v[20:23], v[164:167], v[156:159], v[6:9]
	v_fma_f32 v2, v34, v2, s46
	v_fma_f32 v3, v35, v3, s46
	v_pk_mul_f32 v[2:3], v[2:3], v[34:35] neg_lo:[0,1] neg_hi:[0,1]
	v_mfma_f32_16x16x32_f16 v[6:9], v[176:179], v[156:159], v[16:19]
	v_fma_f32 v2, v2, v30, 1.0
	v_fma_f32 v3, v3, v31, 1.0
	v_bfi_b32 v3, s71, v3, v29
	v_bfi_b32 v2, s71, v2, v28
	v_pk_add_f32 v[2:3], v[2:3], 1.0 op_sel_hi:[1,0]
	s_nop 0
	v_pk_mul_f32 v[4:5], v[26:27], v[2:3]
	v_cvt_pk_f16_f32 v2, v24, v25
	v_cvt_pk_f16_f32 v3, v4, v5
	s_waitcnt lgkmcnt(0)
	v_pk_fma_f32 v[4:5], v[20:21], v[160:161], v[188:189]
	s_nop 0
	v_pk_mul_f32 v[16:17], v[4:5], s[28:29] op_sel_hi:[1,0]
	v_pk_mul_f32 v[4:5], v[4:5], 0.5 op_sel_hi:[1,0]
	v_fma_f32 v18, |v16|, s74, 1.0
	v_fma_f32 v19, |v17|, s74, 1.0
	v_rcp_f32_e32 v18, v18
	v_rcp_f32_e32 v19, v19
	v_mul_f32_e64 v20, |v16|, -|v16|
	v_mul_f32_e64 v21, |v17|, -|v17|
	v_mul_f32_e32 v20, 0x3fb8aa3b, v20
	v_pk_fma_f32 v[24:25], v[18:19], s[40:41], v[14:15] op_sel_hi:[1,0,0]
	v_mul_f32_e32 v21, 0x3fb8aa3b, v21
	v_exp_f32_e32 v20, v20
	v_pk_fma_f32 v[24:25], v[18:19], v[24:25], s[42:43] op_sel_hi:[1,1,0]
	v_exp_f32_e32 v21, v21
	v_pk_fma_f32 v[24:25], v[18:19], v[24:25], s[44:45] op_sel_hi:[1,1,0]
	s_nop 0
	v_pk_fma_f32 v[24:25], v[18:19], v[24:25], s[46:47] op_sel_hi:[1,1,0]
	s_nop 0
	v_pk_mul_f32 v[18:19], v[24:25], v[18:19] neg_lo:[0,1] neg_hi:[0,1]
	s_nop 0
	v_pk_fma_f32 v[18:19], v[18:19], v[20:21], 1.0 op_sel_hi:[1,1,0]
	s_nop 0
	v_bfi_b32 v17, s71, v19, v17
	v_bfi_b32 v16, s71, v18, v16
	v_pk_add_f32 v[16:17], v[16:17], 1.0 op_sel_hi:[1,0]
	s_nop 0
	v_pk_mul_f32 v[4:5], v[4:5], v[16:17]
	v_pk_fma_f32 v[16:17], v[22:23], v[162:163], v[190:191]
	v_cvt_pk_f16_f32 v4, v4, v5
	v_pk_mul_f32 v[18:19], v[16:17], s[28:29] op_sel_hi:[1,0]
	v_pk_mul_f32 v[16:17], v[16:17], 0.5 op_sel_hi:[1,0]
	v_fma_f32 v20, |v18|, s74, 1.0
	v_fma_f32 v21, |v19|, s74, 1.0
	v_rcp_f32_e32 v20, v20
	v_rcp_f32_e32 v21, v21
	v_mul_f32_e64 v22, |v18|, -|v18|
	v_mul_f32_e64 v23, |v19|, -|v19|
	v_mul_f32_e32 v22, 0x3fb8aa3b, v22
	v_pk_fma_f32 v[24:25], v[20:21], s[40:41], v[14:15] op_sel_hi:[1,0,0]
	v_mul_f32_e32 v23, 0x3fb8aa3b, v23
	v_exp_f32_e32 v22, v22
	v_pk_fma_f32 v[24:25], v[20:21], v[24:25], s[42:43] op_sel_hi:[1,1,0]
	v_exp_f32_e32 v23, v23
	v_pk_fma_f32 v[24:25], v[20:21], v[24:25], s[44:45] op_sel_hi:[1,1,0]
	s_nop 0
	v_pk_fma_f32 v[24:25], v[20:21], v[24:25], s[46:47] op_sel_hi:[1,1,0]
	s_nop 0
	v_pk_mul_f32 v[20:21], v[24:25], v[20:21] neg_lo:[0,1] neg_hi:[0,1]
	s_nop 0
	v_pk_fma_f32 v[20:21], v[20:21], v[22:23], 1.0 op_sel_hi:[1,1,0]
	s_nop 0
	v_bfi_b32 v19, s71, v21, v19
	v_bfi_b32 v18, s71, v20, v18
	v_pk_add_f32 v[18:19], v[18:19], 1.0 op_sel_hi:[1,0]
	s_nop 0
	v_pk_mul_f32 v[16:17], v[16:17], v[18:19]
	ds_read_b128 v[18:21], v98 offset:63936
	ds_read_b128 v[22:25], v98 offset:64192
	v_cvt_pk_f16_f32 v5, v16, v17
	ds_read_b128 v[26:29], v98 offset:64000
	ds_read_b128 v[30:33], v98 offset:64256
	s_waitcnt lgkmcnt(2)
	v_pk_fma_f32 v[10:11], v[10:11], v[18:19], v[22:23]
	s_nop 0
	v_pk_mul_f32 v[22:23], v[10:11], s[28:29] op_sel_hi:[1,0]
	v_pk_fma_f32 v[12:13], v[12:13], v[20:21], v[24:25]
	v_fma_f32 v16, |v22|, s74, 1.0
	v_fma_f32 v17, |v23|, s74, 1.0
	v_rcp_f32_e32 v16, v16
	v_rcp_f32_e32 v17, v17
	v_mul_f32_e64 v18, |v22|, -|v22|
	v_mul_f32_e64 v19, |v23|, -|v23|
	v_mul_f32_e32 v18, 0x3fb8aa3b, v18
	v_pk_fma_f32 v[34:35], v[16:17], s[40:41], v[14:15] op_sel_hi:[1,0,0]
	v_mul_f32_e32 v19, 0x3fb8aa3b, v19
	v_exp_f32_e32 v18, v18
	v_pk_fma_f32 v[34:35], v[16:17], v[34:35], s[42:43] op_sel_hi:[1,1,0]
	v_exp_f32_e32 v19, v19
	v_pk_fma_f32 v[34:35], v[16:17], v[34:35], s[44:45] op_sel_hi:[1,1,0]
	v_pk_mul_f32 v[10:11], v[10:11], 0.5 op_sel_hi:[1,0]
	v_pk_fma_f32 v[34:35], v[16:17], v[34:35], s[46:47] op_sel_hi:[1,1,0]
	v_pk_mul_f32 v[20:21], v[12:13], s[28:29] op_sel_hi:[1,0]
	v_pk_mul_f32 v[16:17], v[34:35], v[16:17] neg_lo:[0,1] neg_hi:[0,1]
	v_mul_f32_e64 v24, |v20|, -|v20|
	v_pk_fma_f32 v[46:47], v[16:17], v[18:19], 1.0 op_sel_hi:[1,1,0]
	v_lshl_add_u64 v[18:19], s[50:51], 1, v[100:101]
	global_load_dwordx4 v[34:37], v[18:19], off
	global_load_dwordx4 v[42:45], v[18:19], off offset:1024
	v_lshl_add_u64 v[16:17], s[50:51], 2, v[102:103]
	global_load_dwordx4 v[38:41], v[16:17], off
	v_mov_b32_e32 v190, 0x1000
	v_mov_b32_e32 v191, 0
	global_load_dwordx4 v[152:155], v[18:19], off offset:2048
	global_load_dwordx4 v[156:159], v[18:19], off offset:3072
	global_load_dwordx4 v[160:163], v[16:17], off offset:64
	v_lshl_add_u64 v[188:189], v[18:19], 0, v[190:191]
	global_load_dwordx4 v[164:167], v[188:189], off
	global_load_dwordx4 v[168:171], v[188:189], off offset:1024
	global_load_dwordx4 v[172:175], v[16:17], off offset:128
	global_load_dwordx4 v[176:179], v[188:189], off offset:2048
	global_load_dwordx4 v[180:183], v[188:189], off offset:3072
	global_load_dwordx4 v[184:187], v[16:17], off offset:192
	v_bfi_b32 v23, s71, v47, v23
	v_bfi_b32 v22, s71, v46, v22
	v_pk_add_f32 v[22:23], v[22:23], 1.0 op_sel_hi:[1,0]
	v_mul_f32_e64 v25, |v21|, -|v21|
	v_pk_mul_f32 v[10:11], v[10:11], v[22:23]
	v_fma_f32 v22, |v20|, s74, 1.0
	v_fma_f32 v23, |v21|, s74, 1.0
	v_rcp_f32_e32 v22, v22
	v_rcp_f32_e32 v23, v23
	v_mul_f32_e32 v24, 0x3fb8aa3b, v24
	v_mul_f32_e32 v25, 0x3fb8aa3b, v25
	v_exp_f32_e32 v24, v24
	v_pk_fma_f32 v[46:47], v[22:23], s[40:41], v[14:15] op_sel_hi:[1,0,0]
	v_exp_f32_e32 v25, v25
	v_pk_fma_f32 v[46:47], v[22:23], v[46:47], s[42:43] op_sel_hi:[1,1,0]
	v_pk_mul_f32 v[12:13], v[12:13], 0.5 op_sel_hi:[1,0]
	v_pk_fma_f32 v[46:47], v[22:23], v[46:47], s[44:45] op_sel_hi:[1,1,0]
	s_waitcnt lgkmcnt(0)
	v_pk_fma_f32 v[6:7], v[6:7], v[26:27], v[30:31]
	v_pk_fma_f32 v[46:47], v[22:23], v[46:47], s[46:47] op_sel_hi:[1,1,0]
	v_cvt_pk_f16_f32 v10, v10, v11
	v_pk_mul_f32 v[22:23], v[46:47], v[22:23] neg_lo:[0,1] neg_hi:[0,1]
	v_pk_fma_f32 v[8:9], v[8:9], v[28:29], v[32:33]
	v_pk_fma_f32 v[22:23], v[22:23], v[24:25], 1.0 op_sel_hi:[1,1,0]
	s_mul_i32 s50, s94, 0xfef85000
	v_bfi_b32 v21, s71, v23, v21
	v_bfi_b32 v20, s71, v22, v20
	v_pk_add_f32 v[20:21], v[20:21], 1.0 op_sel_hi:[1,0]
	s_nop 0
	v_pk_mul_f32 v[12:13], v[12:13], v[20:21]
	s_nop 0
	v_cvt_pk_f16_f32 v11, v12, v13
	v_pk_mul_f32 v[12:13], v[6:7], s[28:29] op_sel_hi:[1,0]
	v_pk_mul_f32 v[6:7], v[6:7], 0.5 op_sel_hi:[1,0]
	v_fma_f32 v20, |v12|, s74, 1.0
	v_fma_f32 v21, |v13|, s74, 1.0
	v_rcp_f32_e32 v20, v20
	v_rcp_f32_e32 v21, v21
	v_mul_f32_e64 v22, |v12|, -|v12|
	v_mul_f32_e64 v23, |v13|, -|v13|
	v_mul_f32_e32 v22, 0x3fb8aa3b, v22
	v_pk_fma_f32 v[24:25], v[20:21], s[40:41], v[14:15] op_sel_hi:[1,0,0]
	v_mul_f32_e32 v23, 0x3fb8aa3b, v23
	v_exp_f32_e32 v22, v22
	v_pk_fma_f32 v[24:25], v[20:21], v[24:25], s[42:43] op_sel_hi:[1,1,0]
	v_exp_f32_e32 v23, v23
	v_pk_fma_f32 v[24:25], v[20:21], v[24:25], s[44:45] op_sel_hi:[1,1,0]
	s_nop 0
	v_pk_fma_f32 v[24:25], v[20:21], v[24:25], s[46:47] op_sel_hi:[1,1,0]
	s_nop 0
	v_pk_mul_f32 v[20:21], v[24:25], v[20:21] neg_lo:[0,1] neg_hi:[0,1]
	s_nop 0
	v_pk_fma_f32 v[20:21], v[20:21], v[22:23], 1.0 op_sel_hi:[1,1,0]
	s_nop 0
	v_bfi_b32 v13, s71, v21, v13
	v_bfi_b32 v12, s71, v20, v12
	v_pk_add_f32 v[12:13], v[12:13], 1.0 op_sel_hi:[1,0]
	s_nop 0
	v_pk_mul_f32 v[6:7], v[6:7], v[12:13]
	v_pk_mul_f32 v[12:13], v[8:9], s[28:29] op_sel_hi:[1,0]
	v_pk_mul_f32 v[8:9], v[8:9], 0.5 op_sel_hi:[1,0]
	v_fma_f32 v20, |v12|, s74, 1.0
	v_fma_f32 v21, |v13|, s74, 1.0
	v_rcp_f32_e32 v20, v20
	v_rcp_f32_e32 v21, v21
	v_mul_f32_e64 v22, |v12|, -|v12|
	v_mul_f32_e64 v23, |v13|, -|v13|
	v_mul_f32_e32 v22, 0x3fb8aa3b, v22
	v_pk_fma_f32 v[14:15], v[20:21], s[40:41], v[14:15] op_sel_hi:[1,0,0]
	v_mul_f32_e32 v23, 0x3fb8aa3b, v23
	v_exp_f32_e32 v22, v22
	v_pk_fma_f32 v[14:15], v[20:21], v[14:15], s[42:43] op_sel_hi:[1,1,0]
	v_exp_f32_e32 v23, v23
	v_pk_fma_f32 v[14:15], v[20:21], v[14:15], s[44:45] op_sel_hi:[1,1,0]
	s_nop 0
	v_pk_fma_f32 v[14:15], v[20:21], v[14:15], s[46:47] op_sel_hi:[1,1,0]
	s_nop 0
	v_pk_mul_f32 v[14:15], v[14:15], v[20:21] neg_lo:[0,1] neg_hi:[0,1]
	s_nop 0
	v_pk_fma_f32 v[14:15], v[14:15], v[22:23], 1.0 op_sel_hi:[1,1,0]
	s_nop 0
	v_bfi_b32 v13, s71, v15, v13
	v_bfi_b32 v12, s71, v14, v12
	v_pk_add_f32 v[12:13], v[12:13], 1.0 op_sel_hi:[1,0]
	v_add_u32_e32 v14, s95, v128
	v_pk_mul_f32 v[8:9], v[8:9], v[12:13]
	v_cvt_pk_f16_f32 v12, v6, v7
	v_cvt_pk_f16_f32 v13, v8, v9
	s_waitcnt vmcnt(0)
	v_pk_mul_f32 v[8:9], v[40:41], s[48:49] op_sel_hi:[1,0]
	v_pk_mul_f32 v[6:7], v[38:39], s[48:49] op_sel_hi:[1,0]
	v_cmp_gt_i32_e64 s[20:21], s73, v14
	v_add_u32_e32 v14, s50, v134
	v_mfma_f32_16x16x32_f16 v[6:9], v[34:37], v[2:5], v[6:9]
	v_mfma_f32_16x16x32_f16 v[6:9], v[42:45], v[10:13], v[6:9]
	v_pk_mul_f32 v[160:161], v[160:161], s[48:49] op_sel_hi:[1,0]
	v_pk_mul_f32 v[162:163], v[162:163], s[48:49] op_sel_hi:[1,0]
	v_pk_mul_f32 v[172:173], v[172:173], s[48:49] op_sel_hi:[1,0]
	v_pk_mul_f32 v[174:175], v[174:175], s[48:49] op_sel_hi:[1,0]
	v_pk_mul_f32 v[184:185], v[184:185], s[48:49] op_sel_hi:[1,0]
	v_pk_mul_f32 v[186:187], v[186:187], s[48:49] op_sel_hi:[1,0]
	s_nop 1
	v_mfma_f32_16x16x32_f16 v[20:23], v[152:155], v[2:5], v[160:163]
	v_mfma_f32_16x16x32_f16 v[24:27], v[164:167], v[2:5], v[172:175]
	v_mfma_f32_16x16x32_f16 v[28:31], v[176:179], v[2:5], v[184:187]
	v_mfma_f32_16x16x32_f16 v[20:23], v[156:159], v[10:13], v[20:23]
	v_mfma_f32_16x16x32_f16 v[24:27], v[168:171], v[10:13], v[24:27]
	v_mfma_f32_16x16x32_f16 v[28:31], v[180:183], v[10:13], v[28:31]
	s_and_saveexec_b64 s[50:51], s[20:21]
	s_cbranch_execz .Lmy_k2_nostore
	s_nop 7
	buffer_store_dwordx4 v[6:9], v14, s[24:27], 0 offen sc1
	buffer_store_dwordx4 v[20:23], v14, s[24:27], 0 offen offset:64 sc1
	buffer_store_dwordx4 v[24:27], v14, s[24:27], 0 offen offset:128 sc1
	buffer_store_dwordx4 v[28:31], v14, s[24:27], 0 offen offset:192 sc1
